# stack + NSA compressed-branch staging: four kc/vc loads in flight together
# speedup vs baseline: 1.0054x; 1.0033x over previous
; #define LAS __attribute__((address_space(3)))
; __device__ __forceinline__ int kperm(int key) { return (key & ~12) | ((key & 4) << 1) | ((key & 8) >> 1); }
; __device__ __forceinline__ void unit(LAS unsigned char* lds, const bf16* Z, const bf16* kct, const bf16* vct, bf16* OAp, int b, int g, int iq, const int tid_in) {
;     int tid = tid_in; asm volatile("" : "+v"(tid));
;     const int lane = tid & 63, r32 = lane & 31, hi = lane >> 5; const int w = __builtin_amdgcn_readfirstlane(tid >> 6);
;     const int j = w >> 1, hq = 4 * g + j, tl = 32 * (w & 1) + r32, t0 = 64 * iq, t = t0 + tl;
;     const size_t rowZ = (size_t)(b * T + t) * ZLD;
;     LAS bf16* KS = (LAS bf16*)(lds + L_KS); LAS bf16* VT = (LAS bf16*)(lds + L_VT); LAS bf16* KC = (LAS bf16*)(lds + L_KC); LAS bf16* VC = (LAS bf16*)(lds + L_VC);
;     LAS float* IA = (LAS float*)(lds + L_IA); LAS float* IB = (LAS float*)(lds + L_IB); LAS unsigned* MSK = (LAS unsigned*)(lds + L_MASK); LAS int* TL = (LAS int*)(lds + L_TL);
;     bf16x8 qr[4];
; #pragma unroll
;     for (int d0 = 0; d0 < 4; ++d0) qr[d0] = *(const bf16x8*)(Z + rowZ + ZQ + hq * 64 + 16 * d0 + 8 * hi);
;     const float slope2 = __builtin_amdgcn_exp2f(-0.5f * (float)(hq + 1)) * LOG2E;
;     float gate[3];
; #pragma unroll
;     for (int x = 0; x < 3; ++x) gate[x] = sigmoidf_(bf2f(Z[rowZ + ZNG + hq * 3 + x]));
;     f32x16 otot[2];
; #pragma unroll
;     for (int r = 0; r < 16; ++r) { otot[0][r] = 0.f; otot[1][r] = 0.f; }
;     {
;         const bf16* kc = kct + (size_t)((b * 4 + g) * 128) * 64; const bf16* vc = vct + (size_t)((b * 4 + g) * 128) * 64;
; #pragma unroll
;         for (int q = 0; q < 2; ++q) { const int idx = tid + 512 * q, key = idx >> 3, ch = idx & 7;
;             const v4u kv = *(const v4u*)(kc + key * 64 + ch * 8); *(LAS v4u*)(KC + key * KST + ch * 8) = kv;
;             const v4u vv = *(const v4u*)(vc + key * 64 + ch * 8); const int pos = kperm(key);
;             const unsigned ww[4] = {vv.x, vv.y, vv.z, vv.w};
; #pragma unroll
;             for (int e = 0; e < 4; ++e) { VC[(ch * 8 + 2 * e) * VST2 + pos] = (bf16)(ww[e] & 0xffffu); VC[(ch * 8 + 2 * e + 1) * VST2 + pos] = (bf16)(ww[e] >> 16); } }
;     }
;     __syncthreads();
;     {
;         f32x16 p[4];
; #pragma unroll
;         for (int blk = 0; blk < 4; ++blk) {
; #pragma unroll
;             for (int r = 0; r < 16; ++r) p[blk][r] = 0.f;
; #pragma unroll
.LBB0_416:
	v_mov_b32_e32 v78, v123
	s_and_b32 s23, s4, 3
	s_ashr_i32 s5, s4, 2
	v_readfirstlane_b32 s0, v78
	v_and_b32_e32 v73, 31, v78
	s_ashr_i32 s4, s0, 7
	s_lshl_b32 s1, s23, 2
	s_lshr_b32 s0, s0, 1
	s_add_i32 s6, s4, s1
	v_and_or_b32 v68, s0, 32, v73
	v_readlane_b32 s0, v253, 32
	v_lshl_or_b32 v77, s18, 6, v68
	s_lshl_b32 s22, s5, 11
	v_readlane_b32 s1, v253, 33
	v_or_b32_e32 v118, s22, v77
	s_lshl_b32 s16, s6, 6
	v_mov_b64_e32 v[2:3], s[0:1]
	v_mad_i64_i32 v[2:3], s[0:1], v118, s26, v[2:3]
	s_add_i32 s0, s6, 1
	v_bfe_u32 v74, v78, 5, 1
	s_ashr_i32 s17, s16, 31
	v_cvt_f32_i32_e32 v1, s0
	s_mul_i32 s0, s6, 3
	v_lshl_add_u64 v[4:5], s[16:17], 1, v[2:3]
	v_lshlrev_b32_e32 v120, 4, v74
	v_mov_b32_e32 v121, v187
	s_ashr_i32 s1, s0, 31
	v_lshl_add_u64 v[4:5], v[4:5], 0, v[120:121]
	v_lshl_add_u64 v[2:3], s[0:1], 1, v[2:3]
	s_mov_b64 s[0:1], 0x1400
	global_load_dwordx4 v[98:101], v[4:5], off
	global_load_dwordx4 v[102:105], v[4:5], off offset:32
	global_load_dwordx4 v[106:109], v[4:5], off offset:64
	global_load_dwordx4 v[110:113], v[4:5], off offset:96
	v_lshl_add_u64 v[4:5], v[2:3], 0, s[0:1]
	s_lshl_b32 s0, s5, 9
	s_lshl_b32 s28, s23, 7
	v_add_co_u32_e32 v2, vcc, s97, v2
	s_or_b32 s0, s28, s0
	s_nop 0
	v_addc_co_u32_e32 v3, vcc, 0, v3, vcc
	s_ashr_i32 s1, s0, 31
	global_load_dword v69, v[2:3], off offset:1024
	global_load_ushort v121, v[4:5], off offset:4
	s_lshl_b64 s[0:1], s[0:1], 7
	v_readlane_b32 s5, v252, 0
	v_lshlrev_b32_e32 v2, 3, v78
	v_ashrrev_i32_e32 v119, 3, v78
	s_add_u32 s6, s5, s0
	v_readlane_b32 s5, v252, 1
	v_and_b32_e32 v9, 56, v2
	v_lshlrev_b32_e32 v2, 6, v119
	s_addc_u32 s7, s5, s1
	v_lshlrev_b32_e32 v186, 1, v9
	v_ashrrev_i32_e32 v3, 31, v2
	v_lshl_add_u64 v[6:7], s[6:7], 0, v[186:187]
	v_lshlrev_b64 v[12:13], 1, v[2:3]
	v_lshl_add_u64 v[2:3], v[6:7], 0, v[12:13]
	global_load_dwordx4 v[200:203], v[2:3], off
	v_readlane_b32 s5, v252, 4
	s_add_u32 s0, s5, s0
	v_readlane_b32 s5, v252, 5
	s_addc_u32 s1, s5, s1
	v_add_u32_e32 v8, 0, v186
	s_movk_i32 s5, 0x90
	v_lshl_add_u64 v[10:11], s[0:1], 0, v[186:187]
	v_mad_u64_u32 v[14:15], s[0:1], v119, s5, v[8:9]
	s_movk_i32 s0, 0x10e
	s_nop 0
	v_mad_u32_u24 v9, v9, s0, v8
	v_lshl_add_u64 v[2:3], v[10:11], 0, v[12:13]
	global_load_dwordx4 v[204:207], v[2:3], off
	v_add_u32_e32 v2, 0x200, v78
	v_ashrrev_i32_e32 v15, 3, v2
	v_lshlrev_b32_e32 v2, 6, v15
	v_ashrrev_i32_e32 v3, 31, v2
	v_lshlrev_b64 v[2:3], 1, v[2:3]
	v_lshl_add_u64 v[4:5], v[6:7], 0, v[2:3]
	global_load_dwordx4 v[208:211], v[4:5], off
	v_lshl_add_u64 v[4:5], v[10:11], 0, v[2:3]
	global_load_dwordx4 v[212:215], v[4:5], off
	v_add_u32_e32 v76, 0, v120
	v_mad_u32_u24 v66, v73, s5, v76
	v_mul_f32_e32 v1, -0.5, v1
	v_exp_f32_e32 v1, v1
	v_lshlrev_b32_e32 v122, 2, v74
	v_and_b32_e32 v79, 63, v78
	v_cmp_eq_u32_e64 s[44:45], 0, v73
	v_mul_f32_e32 v124, 0x3fb8aa3b, v1
	v_lshlrev_b32_e32 v5, 1, v119
	v_lshrrev_b32_e32 v12, 1, v119
	v_and_b32_e32 v4, 0x7ffffff3, v119
	v_and_b32_e32 v5, 8, v5
	v_and_b32_e32 v12, 4, v12
	v_or3_b32 v4, v5, v4, v12
	v_lshl_add_u32 v12, v4, 1, v9
	v_mad_u64_u32 v[6:7], s[0:1], v15, s5, v[8:9]
	v_lshlrev_b32_e32 v5, 1, v15
	v_lshrrev_b32_e32 v13, 1, v15
	v_and_b32_e32 v4, 0x7ffffff3, v15
	v_and_b32_e32 v5, 8, v5
	v_and_b32_e32 v13, 4, v13
	v_or3_b32 v4, v5, v4, v13
	v_lshl_add_u32 v13, v4, 1, v9
	s_mov_b32 s5, 0xff800000
	v_cmp_gt_u32_e64 s[0:1], 32, v79
	s_waitcnt vmcnt(3)
	ds_write_b128 v14, v[200:203] offset:18432
	s_waitcnt vmcnt(2)
	ds_write_b16 v12, v204 offset:36864
	ds_write_b16_d16_hi v12, v204 offset:37136
	ds_write_b16 v12, v205 offset:37408
	ds_write_b16_d16_hi v12, v205 offset:37680
	ds_write_b16 v12, v206 offset:37952
	ds_write_b16_d16_hi v12, v206 offset:38224
	ds_write_b16 v12, v207 offset:38496
	ds_write_b16_d16_hi v12, v207 offset:38768
	s_waitcnt vmcnt(1)
	ds_write_b128 v6, v[208:211] offset:18432
	s_waitcnt vmcnt(0)
	ds_write_b16 v13, v212 offset:36864
	ds_write_b16_d16_hi v13, v212 offset:37136
	ds_write_b16 v13, v213 offset:37408
	ds_write_b16_d16_hi v13, v213 offset:37680
	ds_write_b16 v13, v214 offset:37952
	ds_write_b16_d16_hi v13, v214 offset:38224
	ds_write_b16 v13, v215 offset:38496
	ds_write_b16_d16_hi v13, v215 offset:38768
	s_waitcnt lgkmcnt(0)
	s_barrier
	ds_read_b128 v[2:5], v66 offset:18432
	ds_read_b128 v[6:9], v66 offset:18464
	s_waitcnt lgkmcnt(1)
	v_mfma_f32_32x32x16_bf16 v[50:65], v[2:5], v[98:101], 0
	ds_read_b128 v[2:5], v66 offset:18496
	ds_read_b128 v[80:83], v66 offset:32288
	s_waitcnt lgkmcnt(2)
	v_mfma_f32_32x32x16_bf16 v[50:65], v[6:9], v[102:105], v[50:65]
	s_waitcnt lgkmcnt(1)
	v_mfma_f32_32x32x16_bf16 v[50:65], v[2:5], v[106:109], v[50:65]
	ds_read_b128 v[2:5], v66 offset:18528
	s_waitcnt lgkmcnt(0)
	v_mfma_f32_32x32x16_bf16 v[50:65], v[2:5], v[110:113], v[50:65]
	ds_read_b128 v[2:5], v66 offset:23040
	s_waitcnt lgkmcnt(0)
	v_mfma_f32_32x32x16_bf16 v[34:49], v[2:5], v[98:101], 0
	ds_read_b128 v[2:5], v66 offset:23072
	s_waitcnt lgkmcnt(0)
	v_mfma_f32_32x32x16_bf16 v[34:49], v[2:5], v[102:105], v[34:49]
	ds_read_b128 v[2:5], v66 offset:23104
	s_waitcnt lgkmcnt(0)
	v_mfma_f32_32x32x16_bf16 v[34:49], v[2:5], v[106:109], v[34:49]
	ds_read_b128 v[2:5], v66 offset:23136
	s_waitcnt lgkmcnt(0)
	v_mfma_f32_32x32x16_bf16 v[34:49], v[2:5], v[110:113], v[34:49]
	ds_read_b128 v[2:5], v66 offset:27648
	s_waitcnt lgkmcnt(0)
	v_mfma_f32_32x32x16_bf16 v[18:33], v[2:5], v[98:101], 0
	ds_read_b128 v[2:5], v66 offset:27680
	s_waitcnt lgkmcnt(0)
	v_mfma_f32_32x32x16_bf16 v[18:33], v[2:5], v[102:105], v[18:33]
	ds_read_b128 v[2:5], v66 offset:27712
	s_waitcnt lgkmcnt(0)
	v_mfma_f32_32x32x16_bf16 v[18:33], v[2:5], v[106:109], v[18:33]
	ds_read_b128 v[2:5], v66 offset:27744
	s_waitcnt lgkmcnt(0)
; #define LAS __attribute__((address_space(3)))
; __device__ __forceinline__ int crow(int r, int hi) { return (r & 3) + 8 * (r >> 2) + 4 * hi; }
; #define MFMA32(a, b, c) __builtin_amdgcn_mfma_f32_32x32x16_bf16((a), (b), (c), 0, 0, 0)
; __device__ __forceinline__ void unit(LAS unsigned char* lds, const bf16* Z, const bf16* kct, const bf16* vct, bf16* OAp, int b, int g, int iq, const int tid_in) {
;     ...
;             for (int d0 = 0; d0 < 4; ++d0) { const bf16x8 kf = *(const LAS bf16x8*)(KC + (32 * blk + r32) * KST + 16 * d0 + 8 * hi); p[blk] = MFMA32(kf, qr[d0], p[blk]); }
;         }
;         float mx = -INFINITY;
; #pragma unroll
;         for (int blk = 0; blk < 4; ++blk)
; #pragma unroll
;             for (int r = 0; r < 16; ++r) { const int c = 32 * blk + crow(r, hi); const int dist = t - (16 * c + 31); const bool ok = (dist >= 0) && (c < 127);
;                 const float s = ok ? p[blk][r] - slope2 * (float)dist : -INFINITY; p[blk][r] = s; mx = fmaxf(mx, s); }
	v_mfma_f32_32x32x16_bf16 v[18:33], v[2:5], v[110:113], v[18:33]
	ds_read_b128 v[2:5], v66 offset:32256
	s_waitcnt lgkmcnt(0)
	v_mfma_f32_32x32x16_bf16 v[2:17], v[2:5], v[98:101], 0
	v_mfma_f32_32x32x16_bf16 v[2:17], v[80:83], v[102:105], v[2:17]
	ds_read_b128 v[80:83], v66 offset:32320
	s_waitcnt lgkmcnt(0)
	v_mfma_f32_32x32x16_bf16 v[2:17], v[80:83], v[106:109], v[2:17]
	ds_read_b128 v[80:83], v66 offset:32352
	s_waitcnt lgkmcnt(0)
	v_mfma_f32_32x32x16_bf16 v[2:17], v[80:83], v[110:113], v[2:17]
	v_subrev_u32_e32 v80, 31, v77
	v_lshlrev_b32_e32 v81, 6, v74
	v_sub_u32_e32 v1, v80, v81
	v_cmp_lt_i32_e32 vcc, -1, v1
	v_cvt_f32_u32_e32 v1, v1
	v_fma_f32 v1, -v124, v1, v50
	v_cndmask_b32_e32 v66, v229, v1, vcc
	v_or_b32_e32 v1, 16, v81
	v_sub_u32_e32 v1, v80, v1
	v_cmp_lt_i32_e32 vcc, -1, v1
	v_cvt_f32_u32_e32 v1, v1
	v_or_b32_e32 v50, 2, v122
	v_lshlrev_b32_e32 v71, 4, v50
	v_sub_u32_e32 v71, v80, v71
	v_fma_f32 v1, -v124, v1, v51
	v_cndmask_b32_e32 v67, v229, v1, vcc
	v_cmp_lt_i32_e32 vcc, -1, v71
	v_cvt_f32_u32_e32 v71, v71
	v_or_b32_e32 v1, 3, v122
	v_max3_f32 v70, v66, s5, v67
	v_mov_b32_e32 v51, v122
	v_fma_f32 v52, -v124, v71, v52
	v_lshlrev_b32_e32 v71, 4, v1
	v_sub_u32_e32 v71, v80, v71
	v_cndmask_b32_e32 v52, v229, v52, vcc
	v_cmp_lt_i32_e32 vcc, -1, v71
	v_cvt_f32_u32_e32 v71, v71
	v_fma_f32 v53, -v124, v71, v53
	v_cndmask_b32_e32 v53, v229, v53, vcc
	v_max3_f32 v71, v70, v52, v53
	v_or_b32_e32 v70, 8, v122
	v_lshlrev_b32_e32 v72, 4, v70
	v_sub_u32_e32 v72, v80, v72
	v_cmp_lt_i32_e32 vcc, -1, v72
	v_cvt_f32_u32_e32 v72, v72
	v_fma_f32 v54, -v124, v72, v54
	v_or_b32_e32 v72, 0x90, v81
	v_sub_u32_e32 v72, v80, v72
	v_cndmask_b32_e32 v54, v229, v54, vcc
	v_cmp_lt_i32_e32 vcc, -1, v72
	v_cvt_f32_u32_e32 v72, v72
	v_fma_f32 v55, -v124, v72, v55
	v_or_b32_e32 v72, 0xa0, v81
	v_sub_u32_e32 v72, v80, v72
	v_cndmask_b32_e32 v55, v229, v55, vcc
	v_cmp_lt_i32_e32 vcc, -1, v72
	v_cvt_f32_u32_e32 v72, v72
	v_max3_f32 v71, v71, v54, v55
	v_fma_f32 v56, -v124, v72, v56
	v_or_b32_e32 v72, 0xb0, v81
	v_sub_u32_e32 v72, v80, v72
	v_cndmask_b32_e32 v56, v229, v56, vcc
	v_cmp_lt_i32_e32 vcc, -1, v72
	v_cvt_f32_u32_e32 v72, v72
	v_fma_f32 v57, -v124, v72, v57
	v_cndmask_b32_e32 v57, v229, v57, vcc
	v_max3_f32 v72, v71, v56, v57
	v_or_b32_e32 v71, 16, v122
	v_lshlrev_b32_e32 v75, 4, v71
	v_sub_u32_e32 v75, v80, v75
	v_cmp_lt_i32_e32 vcc, -1, v75
	v_cvt_f32_u32_e32 v75, v75
	v_fma_f32 v58, -v124, v75, v58
	v_or_b32_e32 v75, 0x110, v81
	v_sub_u32_e32 v75, v80, v75
	v_cndmask_b32_e32 v58, v229, v58, vcc
	v_cmp_lt_i32_e32 vcc, -1, v75
	v_cvt_f32_u32_e32 v75, v75
	v_fma_f32 v59, -v124, v75, v59
	v_or_b32_e32 v75, 0x120, v81
	v_sub_u32_e32 v75, v80, v75
	v_cndmask_b32_e32 v59, v229, v59, vcc
	v_cmp_lt_i32_e32 vcc, -1, v75
	v_cvt_f32_u32_e32 v75, v75
	v_max3_f32 v72, v72, v58, v59
	v_fma_f32 v60, -v124, v75, v60
	v_or_b32_e32 v75, 0x130, v81
	v_sub_u32_e32 v75, v80, v75
	v_cndmask_b32_e32 v60, v229, v60, vcc
	v_cmp_lt_i32_e32 vcc, -1, v75
	v_cvt_f32_u32_e32 v75, v75
	v_fma_f32 v61, -v124, v75, v61
	v_cndmask_b32_e32 v61, v229, v61, vcc
	v_max3_f32 v75, v72, v60, v61
	v_or_b32_e32 v72, 24, v122
	v_lshlrev_b32_e32 v82, 4, v72
	v_sub_u32_e32 v82, v80, v82
	v_cmp_lt_i32_e32 vcc, -1, v82
	v_cvt_f32_u32_e32 v82, v82
	v_fma_f32 v62, -v124, v82, v62
	v_or_b32_e32 v82, 0x190, v81
	v_sub_u32_e32 v82, v80, v82
	v_cndmask_b32_e32 v62, v229, v62, vcc
	v_cmp_lt_i32_e32 vcc, -1, v82
	v_cvt_f32_u32_e32 v82, v82
	v_fma_f32 v63, -v124, v82, v63
	v_or_b32_e32 v82, 0x1a0, v81
	v_sub_u32_e32 v82, v80, v82
	v_cndmask_b32_e32 v63, v229, v63, vcc
	v_cmp_lt_i32_e32 vcc, -1, v82
	v_cvt_f32_u32_e32 v82, v82
	v_max3_f32 v75, v75, v62, v63
	v_fma_f32 v64, -v124, v82, v64
	v_or_b32_e32 v82, 0x1b0, v81
	v_sub_u32_e32 v82, v80, v82
	v_cndmask_b32_e32 v64, v229, v64, vcc
	v_cmp_lt_i32_e32 vcc, -1, v82
	v_cvt_f32_u32_e32 v82, v82
	v_fma_f32 v65, -v124, v82, v65
	v_cndmask_b32_e32 v65, v229, v65, vcc
	v_max3_f32 v82, v75, v64, v65
	v_or_b32_e32 v75, 32, v122
	v_lshlrev_b32_e32 v83, 4, v75
	v_sub_u32_e32 v83, v80, v83
	v_cmp_lt_i32_e32 vcc, -1, v83
	v_cvt_f32_u32_e32 v83, v83
	v_fma_f32 v34, -v124, v83, v34
	v_or_b32_e32 v83, 0x210, v81
	v_sub_u32_e32 v83, v80, v83
	v_cndmask_b32_e32 v34, v229, v34, vcc
	v_cmp_lt_i32_e32 vcc, -1, v83
	v_cvt_f32_u32_e32 v83, v83
	v_fma_f32 v35, -v124, v83, v35
	v_or_b32_e32 v83, 0x220, v81
	v_sub_u32_e32 v83, v80, v83
	v_cndmask_b32_e32 v35, v229, v35, vcc
	v_cmp_lt_i32_e32 vcc, -1, v83
	v_cvt_f32_u32_e32 v83, v83
	v_max3_f32 v82, v82, v34, v35
	v_fma_f32 v36, -v124, v83, v36
	v_or_b32_e32 v83, 0x230, v81
	v_sub_u32_e32 v83, v80, v83
	v_cndmask_b32_e32 v36, v229, v36, vcc
	v_cmp_lt_i32_e32 vcc, -1, v83
	v_cvt_f32_u32_e32 v83, v83
	v_fma_f32 v37, -v124, v83, v37
	v_or_b32_e32 v83, 0x280, v81
	v_sub_u32_e32 v83, v80, v83
	v_cndmask_b32_e32 v37, v229, v37, vcc
	v_cmp_lt_i32_e32 vcc, -1, v83
	v_cvt_f32_u32_e32 v83, v83
	v_max3_f32 v82, v82, v36, v37
	v_fma_f32 v38, -v124, v83, v38
	v_or_b32_e32 v83, 0x290, v81
	v_sub_u32_e32 v83, v80, v83
	v_cndmask_b32_e32 v38, v229, v38, vcc
	v_cmp_lt_i32_e32 vcc, -1, v83
	v_cvt_f32_u32_e32 v83, v83
	v_fma_f32 v39, -v124, v83, v39
	v_or_b32_e32 v83, 0x2a0, v81
	v_sub_u32_e32 v83, v80, v83
	v_cndmask_b32_e32 v39, v229, v39, vcc
	v_cmp_lt_i32_e32 vcc, -1, v83
	v_cvt_f32_u32_e32 v83, v83
	v_max3_f32 v82, v82, v38, v39
	v_fma_f32 v40, -v124, v83, v40
	v_or_b32_e32 v83, 0x2b0, v81
	v_sub_u32_e32 v83, v80, v83
	v_cndmask_b32_e32 v40, v229, v40, vcc
	v_cmp_lt_i32_e32 vcc, -1, v83
	v_cvt_f32_u32_e32 v83, v83
	v_fma_f32 v41, -v124, v83, v41
	v_or_b32_e32 v83, 0x300, v81
	v_sub_u32_e32 v83, v80, v83
	v_cndmask_b32_e32 v41, v229, v41, vcc
; __device__ __forceinline__ int crow(int r, int hi) { return (r & 3) + 8 * (r >> 2) + 4 * hi; }
; __device__ __forceinline__ void unit(LAS unsigned char* lds, const bf16* Z, const bf16* kct, const bf16* vct, bf16* OAp, int b, int g, int iq, const int tid_in) {
;     ...
;             for (int r = 0; r < 16; ++r) { const int c = 32 * blk + crow(r, hi); const int dist = t - (16 * c + 31); const bool ok = (dist >= 0) && (c < 127);
;                 const float s = ok ? p[blk][r] - slope2 * (float)dist : -INFINITY; p[blk][r] = s; mx = fmaxf(mx, s); }
	v_cmp_lt_i32_e32 vcc, -1, v83
	v_cvt_f32_u32_e32 v83, v83
	v_max3_f32 v82, v82, v40, v41
	v_fma_f32 v42, -v124, v83, v42
	v_or_b32_e32 v83, 0x310, v81
	v_sub_u32_e32 v83, v80, v83
	v_cndmask_b32_e32 v42, v229, v42, vcc
	v_cmp_lt_i32_e32 vcc, -1, v83
	v_cvt_f32_u32_e32 v83, v83
	v_fma_f32 v43, -v124, v83, v43
	v_or_b32_e32 v83, 0x320, v81
	v_sub_u32_e32 v83, v80, v83
	v_cndmask_b32_e32 v43, v229, v43, vcc
	v_cmp_lt_i32_e32 vcc, -1, v83
	v_cvt_f32_u32_e32 v83, v83
	v_max3_f32 v82, v82, v42, v43
	v_fma_f32 v44, -v124, v83, v44
	v_or_b32_e32 v83, 0x330, v81
	v_sub_u32_e32 v83, v80, v83
	v_cndmask_b32_e32 v44, v229, v44, vcc
	v_cmp_lt_i32_e32 vcc, -1, v83
	v_cvt_f32_u32_e32 v83, v83
	v_fma_f32 v45, -v124, v83, v45
	v_or_b32_e32 v83, 0x380, v81
	v_sub_u32_e32 v83, v80, v83
	v_cndmask_b32_e32 v45, v229, v45, vcc
	v_cmp_lt_i32_e32 vcc, -1, v83
	v_cvt_f32_u32_e32 v83, v83
	v_max3_f32 v82, v82, v44, v45
	v_fma_f32 v46, -v124, v83, v46
	v_or_b32_e32 v83, 0x390, v81
	v_sub_u32_e32 v83, v80, v83
	v_cndmask_b32_e32 v46, v229, v46, vcc
	v_cmp_lt_i32_e32 vcc, -1, v83
	v_cvt_f32_u32_e32 v83, v83
	v_fma_f32 v47, -v124, v83, v47
	v_or_b32_e32 v83, 0x3a0, v81
	v_sub_u32_e32 v83, v80, v83
	v_cndmask_b32_e32 v47, v229, v47, vcc
	v_cmp_lt_i32_e32 vcc, -1, v83
	v_cvt_f32_u32_e32 v83, v83
	v_max3_f32 v82, v82, v46, v47
	v_fma_f32 v48, -v124, v83, v48
	v_or_b32_e32 v83, 0x3b0, v81
	v_sub_u32_e32 v83, v80, v83
	v_cndmask_b32_e32 v48, v229, v48, vcc
	v_cmp_lt_i32_e32 vcc, -1, v83
	v_cvt_f32_u32_e32 v83, v83
	v_fma_f32 v49, -v124, v83, v49
	v_cndmask_b32_e32 v49, v229, v49, vcc
	v_max3_f32 v84, v82, v48, v49
	v_or_b32_e32 v82, 0x400, v81
	v_sub_u32_e32 v82, v80, v82
	v_cmp_lt_i32_e32 vcc, -1, v82
	v_cvt_f32_u32_e32 v82, v82
	v_fma_f32 v18, -v124, v82, v18
	v_cndmask_b32_e32 v82, v229, v18, vcc
	v_or_b32_e32 v18, 0x410, v81
	v_sub_u32_e32 v18, v80, v18
	v_cmp_lt_i32_e32 vcc, -1, v18
	v_cvt_f32_u32_e32 v18, v18
	v_fma_f32 v18, -v124, v18, v19
	v_or_b32_e32 v19, 0x420, v81
	v_sub_u32_e32 v19, v80, v19
	v_cndmask_b32_e32 v83, v229, v18, vcc
	v_cmp_lt_i32_e32 vcc, -1, v19
	v_cvt_f32_u32_e32 v19, v19
	v_max3_f32 v18, v84, v82, v83
	v_fma_f32 v19, -v124, v19, v20
	v_cndmask_b32_e32 v84, v229, v19, vcc
	v_or_b32_e32 v19, 0x430, v81
	v_sub_u32_e32 v19, v80, v19
	v_cmp_lt_i32_e32 vcc, -1, v19
	v_cvt_f32_u32_e32 v19, v19
	v_fma_f32 v19, -v124, v19, v21
	v_cndmask_b32_e32 v85, v229, v19, vcc
	v_or_b32_e32 v19, 0x480, v81
	v_sub_u32_e32 v19, v80, v19
	v_cmp_lt_i32_e32 vcc, -1, v19
	v_cvt_f32_u32_e32 v19, v19
	v_max3_f32 v18, v18, v84, v85
	v_fma_f32 v19, -v124, v19, v22
	v_cndmask_b32_e32 v86, v229, v19, vcc
	v_or_b32_e32 v19, 0x490, v81
	v_sub_u32_e32 v19, v80, v19
	v_cmp_lt_i32_e32 vcc, -1, v19
	v_cvt_f32_u32_e32 v19, v19
	v_fma_f32 v19, -v124, v19, v23
	v_cndmask_b32_e32 v87, v229, v19, vcc
	v_or_b32_e32 v19, 0x4a0, v81
	v_sub_u32_e32 v19, v80, v19
	v_cmp_lt_i32_e32 vcc, -1, v19
	v_cvt_f32_u32_e32 v19, v19
	v_max3_f32 v18, v18, v86, v87
	v_fma_f32 v19, -v124, v19, v24
	v_cndmask_b32_e32 v24, v229, v19, vcc
	v_or_b32_e32 v19, 0x4b0, v81
	v_sub_u32_e32 v19, v80, v19
	v_cmp_lt_i32_e32 vcc, -1, v19
	v_cvt_f32_u32_e32 v19, v19
	v_fma_f32 v19, -v124, v19, v25
	v_cndmask_b32_e32 v25, v229, v19, vcc
	v_or_b32_e32 v19, 0x500, v81
	v_sub_u32_e32 v19, v80, v19
	v_cmp_lt_i32_e32 vcc, -1, v19
	v_cvt_f32_u32_e32 v19, v19
	v_max3_f32 v18, v18, v24, v25
	v_fma_f32 v19, -v124, v19, v26
	v_cndmask_b32_e32 v26, v229, v19, vcc
	v_or_b32_e32 v19, 0x510, v81
	v_sub_u32_e32 v19, v80, v19
	v_cmp_lt_i32_e32 vcc, -1, v19
	v_cvt_f32_u32_e32 v19, v19
	v_fma_f32 v19, -v124, v19, v27
	v_cndmask_b32_e32 v27, v229, v19, vcc
	v_or_b32_e32 v19, 0x520, v81
	v_sub_u32_e32 v19, v80, v19
	v_cmp_lt_i32_e32 vcc, -1, v19
	v_cvt_f32_u32_e32 v19, v19
	v_max3_f32 v18, v18, v26, v27
	v_fma_f32 v19, -v124, v19, v28
	v_cndmask_b32_e32 v28, v229, v19, vcc
	v_or_b32_e32 v19, 0x530, v81
	v_sub_u32_e32 v19, v80, v19
	v_cmp_lt_i32_e32 vcc, -1, v19
	v_cvt_f32_u32_e32 v19, v19
	v_fma_f32 v19, -v124, v19, v29
	v_cndmask_b32_e32 v29, v229, v19, vcc
	v_or_b32_e32 v19, 0x580, v81
	v_sub_u32_e32 v19, v80, v19
	v_cmp_lt_i32_e32 vcc, -1, v19
	v_cvt_f32_u32_e32 v19, v19
	v_max3_f32 v18, v18, v28, v29
	v_fma_f32 v19, -v124, v19, v30
	v_cndmask_b32_e32 v30, v229, v19, vcc
	v_or_b32_e32 v19, 0x590, v81
	v_sub_u32_e32 v19, v80, v19
	v_cmp_lt_i32_e32 vcc, -1, v19
	v_cvt_f32_u32_e32 v19, v19
	v_fma_f32 v19, -v124, v19, v31
	v_cndmask_b32_e32 v31, v229, v19, vcc
	v_or_b32_e32 v19, 0x5a0, v81
	v_sub_u32_e32 v19, v80, v19
	v_cmp_lt_i32_e32 vcc, -1, v19
	v_cvt_f32_u32_e32 v19, v19
	v_max3_f32 v18, v18, v30, v31
	v_fma_f32 v19, -v124, v19, v32
	v_cndmask_b32_e32 v32, v229, v19, vcc
	v_or_b32_e32 v19, 0x5b0, v81
	v_sub_u32_e32 v19, v80, v19
	v_cmp_lt_i32_e32 vcc, -1, v19
	v_cvt_f32_u32_e32 v19, v19
	v_fma_f32 v19, -v124, v19, v33
	v_cndmask_b32_e32 v33, v229, v19, vcc
	v_or_b32_e32 v19, 0x600, v81
	v_sub_u32_e32 v19, v80, v19
	v_cmp_lt_i32_e32 vcc, -1, v19
	v_cvt_f32_u32_e32 v19, v19
	v_max3_f32 v18, v18, v32, v33
	v_fma_f32 v2, -v124, v19, v2
	v_cndmask_b32_e32 v88, v229, v2, vcc
	v_or_b32_e32 v2, 0x610, v81
	v_sub_u32_e32 v2, v80, v2
	v_cmp_lt_i32_e32 vcc, -1, v2
	v_cvt_f32_u32_e32 v2, v2
	v_fma_f32 v2, -v124, v2, v3
	v_or_b32_e32 v3, 0x620, v81
	v_sub_u32_e32 v3, v80, v3
	v_cndmask_b32_e32 v89, v229, v2, vcc
	v_cmp_lt_i32_e32 vcc, -1, v3
	v_cvt_f32_u32_e32 v3, v3
	v_max3_f32 v2, v18, v88, v89
	v_fma_f32 v3, -v124, v3, v4
	v_cndmask_b32_e32 v90, v229, v3, vcc
	v_or_b32_e32 v3, 0x630, v81
	v_sub_u32_e32 v3, v80, v3
	v_cmp_lt_i32_e32 vcc, -1, v3
	v_cvt_f32_u32_e32 v3, v3
	v_and_b32_e32 v4, 64, v228
	v_fma_f32 v3, -v124, v3, v5
; __device__ __forceinline__ int crow(int r, int hi) { return (r & 3) + 8 * (r >> 2) + 4 * hi; }
; __device__ __forceinline__ void unit(LAS unsigned char* lds, const bf16* Z, const bf16* kct, const bf16* vct, bf16* OAp, int b, int g, int iq, const int tid_in) {
;     ...
;             for (int r = 0; r < 16; ++r) { const int c = 32 * blk + crow(r, hi); const int dist = t - (16 * c + 31); const bool ok = (dist >= 0) && (c < 127);
;                 const float s = ok ? p[blk][r] - slope2 * (float)dist : -INFINITY; p[blk][r] = s; mx = fmaxf(mx, s); }
;         mx = fmaxf(mx, __shfl_xor(mx, 32));
;         const float msafe = (mx == -INFINITY) ? 0.f : mx;
;         float l = 0.f;
; #pragma unroll
;         for (int blk = 0; blk < 4; ++blk)
; #pragma unroll
;             for (int r = 0; r < 16; ++r) { const float e = __builtin_amdgcn_exp2f(p[blk][r] - msafe); p[blk][r] = e; l += e; }
	v_cndmask_b32_e32 v91, v229, v3, vcc
	v_or_b32_e32 v3, 0x680, v81
	v_sub_u32_e32 v3, v80, v3
	v_cmp_lt_i32_e32 vcc, -1, v3
	v_cvt_f32_u32_e32 v3, v3
	v_max3_f32 v2, v2, v90, v91
	v_fma_f32 v3, -v124, v3, v6
	v_cndmask_b32_e32 v92, v229, v3, vcc
	v_or_b32_e32 v3, 0x690, v81
	v_sub_u32_e32 v3, v80, v3
	v_cmp_lt_i32_e32 vcc, -1, v3
	v_cvt_f32_u32_e32 v3, v3
	v_fma_f32 v3, -v124, v3, v7
	v_cndmask_b32_e32 v93, v229, v3, vcc
	v_or_b32_e32 v3, 0x6a0, v81
	v_sub_u32_e32 v3, v80, v3
	v_cmp_lt_i32_e32 vcc, -1, v3
	v_cvt_f32_u32_e32 v3, v3
	v_max3_f32 v2, v2, v92, v93
	v_fma_f32 v3, -v124, v3, v8
	v_cndmask_b32_e32 v94, v229, v3, vcc
	v_or_b32_e32 v3, 0x6b0, v81
	v_sub_u32_e32 v3, v80, v3
	v_cmp_lt_i32_e32 vcc, -1, v3
	v_cvt_f32_u32_e32 v3, v3
	v_fma_f32 v3, -v124, v3, v9
	v_cndmask_b32_e32 v95, v229, v3, vcc
	v_or_b32_e32 v3, 0x700, v81
	v_sub_u32_e32 v3, v80, v3
	v_cmp_lt_i32_e32 vcc, -1, v3
	v_cvt_f32_u32_e32 v3, v3
	v_max3_f32 v2, v2, v94, v95
	v_fma_f32 v3, -v124, v3, v10
	v_cndmask_b32_e32 v96, v229, v3, vcc
	v_or_b32_e32 v3, 0x710, v81
	v_sub_u32_e32 v3, v80, v3
	v_cmp_lt_i32_e32 vcc, -1, v3
	v_cvt_f32_u32_e32 v3, v3
	v_fma_f32 v3, -v124, v3, v11
	v_cndmask_b32_e32 v97, v229, v3, vcc
	v_or_b32_e32 v3, 0x720, v81
	v_sub_u32_e32 v3, v80, v3
	v_cmp_lt_i32_e32 vcc, -1, v3
	v_cvt_f32_u32_e32 v3, v3
	v_max3_f32 v2, v2, v96, v97
	v_fma_f32 v3, -v124, v3, v12
	v_cndmask_b32_e32 v114, v229, v3, vcc
	v_or_b32_e32 v3, 0x730, v81
	v_sub_u32_e32 v3, v80, v3
	v_cmp_lt_i32_e32 vcc, -1, v3
	v_cvt_f32_u32_e32 v3, v3
	v_fma_f32 v3, -v124, v3, v13
	v_cndmask_b32_e32 v115, v229, v3, vcc
	v_or_b32_e32 v3, 0x780, v81
	v_sub_u32_e32 v3, v80, v3
	v_cmp_lt_i32_e32 vcc, -1, v3
	v_cvt_f32_u32_e32 v3, v3
	v_max3_f32 v2, v2, v114, v115
	v_fma_f32 v3, -v124, v3, v14
	v_cndmask_b32_e32 v116, v229, v3, vcc
	v_or_b32_e32 v3, 0x790, v81
	v_sub_u32_e32 v3, v80, v3
	v_cmp_lt_i32_e32 vcc, -1, v3
	v_cvt_f32_u32_e32 v3, v3
	v_fma_f32 v3, -v124, v3, v15
	v_cndmask_b32_e32 v117, v229, v3, vcc
	v_or_b32_e32 v3, 0x7a0, v81
	v_sub_u32_e32 v3, v80, v3
	v_cmp_lt_i32_e32 vcc, -1, v3
	v_cvt_f32_u32_e32 v3, v3
	v_max3_f32 v2, v2, v116, v117
	v_fma_f32 v3, -v124, v3, v16
	v_cndmask_b32_e32 v125, v229, v3, vcc
	v_or_b32_e32 v3, 0x7b0, v81
	v_sub_u32_e32 v3, v80, v3
	v_cmp_lt_i32_e32 vcc, -1, v3
	v_cvt_f32_u32_e32 v3, v3
	s_and_b64 vcc, s[0:1], vcc
	v_add_u32_e32 v80, 64, v4
	v_fma_f32 v3, -v124, v3, v17
	v_cndmask_b32_e32 v81, v229, v3, vcc
	v_xor_b32_e32 v3, 32, v228
	v_cmp_lt_i32_e32 vcc, v3, v80
	v_max3_f32 v2, v2, v125, v81
	s_nop 0
	v_cndmask_b32_e32 v3, v228, v3, vcc
	v_lshlrev_b32_e32 v172, 2, v3
	ds_bpermute_b32 v3, v172, v2
	s_waitcnt lgkmcnt(0)
	v_max_f32_e32 v3, v3, v3
	v_max_f32_e32 v2, v2, v3
	v_cmp_neq_f32_e32 vcc, s5, v2
	s_nop 1
	v_cndmask_b32_e32 v126, 0, v2, vcc
	v_sub_f32_e32 v4, v52, v126
	v_sub_f32_e32 v52, v88, v126
	v_sub_f32_e32 v22, v38, v126
	v_sub_f32_e32 v38, v44, v126
	v_sub_f32_e32 v44, v82, v126
	v_exp_f32_e32 v82, v52
	v_sub_f32_e32 v52, v89, v126
	v_sub_f32_e32 v23, v39, v126
	v_sub_f32_e32 v39, v45, v126
	v_sub_f32_e32 v45, v83, v126
	v_exp_f32_e32 v83, v52
	v_sub_f32_e32 v52, v90, v126
	v_sub_f32_e32 v18, v34, v126
	v_sub_f32_e32 v34, v40, v126
	v_sub_f32_e32 v40, v46, v126
	v_sub_f32_e32 v46, v84, v126
	v_exp_f32_e32 v84, v52
	v_sub_f32_e32 v52, v91, v126
	v_sub_f32_e32 v19, v35, v126
	v_sub_f32_e32 v35, v41, v126
	v_sub_f32_e32 v41, v47, v126
	v_sub_f32_e32 v47, v85, v126
	v_exp_f32_e32 v85, v52
	v_sub_f32_e32 v52, v92, v126
	v_sub_f32_e32 v20, v36, v126
	v_sub_f32_e32 v36, v42, v126
	v_sub_f32_e32 v42, v48, v126
	v_sub_f32_e32 v48, v86, v126
	v_exp_f32_e32 v86, v52
	v_sub_f32_e32 v52, v93, v126
	v_sub_f32_e32 v21, v37, v126
	v_sub_f32_e32 v37, v43, v126
	v_sub_f32_e32 v43, v49, v126
	v_sub_f32_e32 v49, v87, v126
	v_exp_f32_e32 v87, v52
	v_sub_f32_e32 v52, v94, v126
	v_exp_f32_e32 v88, v52
	v_sub_f32_e32 v52, v95, v126
	v_exp_f32_e32 v89, v52
	v_sub_f32_e32 v52, v96, v126
	v_exp_f32_e32 v90, v52
	v_sub_f32_e32 v52, v97, v126
	v_exp_f32_e32 v91, v52
	v_sub_f32_e32 v52, v114, v126
	v_sub_f32_e32 v2, v66, v126
	v_exp_f32_e32 v92, v52
	v_sub_f32_e32 v52, v115, v126
	v_exp_f32_e32 v2, v2
	v_sub_f32_e32 v3, v67, v126
	v_exp_f32_e32 v93, v52
	v_sub_f32_e32 v52, v116, v126
	v_exp_f32_e32 v3, v3
	v_exp_f32_e32 v94, v52
	v_sub_f32_e32 v52, v117, v126
	v_exp_f32_e32 v4, v4
	v_sub_f32_e32 v5, v53, v126
	v_exp_f32_e32 v95, v52
	v_sub_f32_e32 v52, v125, v126
	v_exp_f32_e32 v5, v5
	v_sub_f32_e32 v6, v54, v126
	v_exp_f32_e32 v96, v52
	v_sub_f32_e32 v52, v81, v126
	v_exp_f32_e32 v6, v6
	v_sub_f32_e32 v7, v55, v126
	v_exp_f32_e32 v97, v52
	v_add_f32_e32 v52, 0, v2
	v_exp_f32_e32 v7, v7
	v_sub_f32_e32 v8, v56, v126
	v_add_f32_e32 v52, v3, v52
	v_exp_f32_e32 v8, v8
	v_sub_f32_e32 v9, v57, v126
	v_add_f32_e32 v52, v4, v52
	v_exp_f32_e32 v9, v9
	v_sub_f32_e32 v10, v58, v126
	v_add_f32_e32 v52, v5, v52
	v_exp_f32_e32 v10, v10
	v_sub_f32_e32 v11, v59, v126
	v_add_f32_e32 v52, v6, v52
	v_exp_f32_e32 v11, v11
	v_sub_f32_e32 v12, v60, v126
	v_add_f32_e32 v52, v7, v52
	v_exp_f32_e32 v12, v12
	v_sub_f32_e32 v13, v61, v126
	v_add_f32_e32 v52, v8, v52
	v_exp_f32_e32 v13, v13
	v_sub_f32_e32 v14, v62, v126
	v_add_f32_e32 v52, v9, v52
	v_exp_f32_e32 v14, v14
	v_sub_f32_e32 v15, v63, v126
	v_add_f32_e32 v52, v10, v52
	v_exp_f32_e32 v15, v15
	v_sub_f32_e32 v16, v64, v126
	v_add_f32_e32 v52, v11, v52
	v_exp_f32_e32 v16, v16
	v_sub_f32_e32 v17, v65, v126
	v_add_f32_e32 v52, v12, v52
	v_exp_f32_e32 v17, v17
	v_add_f32_e32 v52, v13, v52
	v_exp_f32_e32 v18, v18
	v_add_f32_e32 v52, v14, v52
	v_exp_f32_e32 v19, v19
	v_add_f32_e32 v52, v15, v52
	v_exp_f32_e32 v20, v20
	v_add_f32_e32 v52, v16, v52
; __device__ __forceinline__ void unit(LAS unsigned char* lds, const bf16* Z, const bf16* kct, const bf16* vct, bf16* OAp, int b, int g, int iq, const int tid_in) {
;     ...
;             for (int r = 0; r < 16; ++r) { const float e = __builtin_amdgcn_exp2f(p[blk][r] - msafe); p[blk][r] = e; l += e; }
;         l += __shfl_xor(l, 32);
;         const float inv = l > 0.f ? 1.0f / l : 0.f;
; #pragma unroll
;         for (int blk = 0; blk < 4; ++blk)
; #pragma unroll
;             for (int r = 0; r < 16; ++r) p[blk][r] *= inv;
; #pragma unroll
;         for (int blk = 0; blk < 4; ++blk)
; #pragma unroll
;             for (int rq = 0; rq < 4; ++rq) { const int n = 8 * blk + 2 * rq + hi;
;                 IA[(j * 64 + tl) * 32 + n] = 2.f * (p[blk][4 * rq] + p[blk][4 * rq + 1] + p[blk][4 * rq + 2]) + p[blk][4 * rq + 3];
;                 IB[(j * 64 + tl) * 32 + n] = p[blk][4 * rq + 3]; }
	v_exp_f32_e32 v21, v21
	v_add_f32_e32 v52, v17, v52
	v_exp_f32_e32 v22, v22
	v_add_f32_e32 v52, v18, v52
	v_exp_f32_e32 v23, v23
	v_add_f32_e32 v52, v19, v52
	v_exp_f32_e32 v34, v34
	v_add_f32_e32 v52, v20, v52
	v_exp_f32_e32 v35, v35
	v_add_f32_e32 v52, v21, v52
	v_exp_f32_e32 v36, v36
	v_add_f32_e32 v52, v22, v52
	v_exp_f32_e32 v37, v37
	v_add_f32_e32 v52, v23, v52
	v_exp_f32_e32 v38, v38
	v_add_f32_e32 v52, v34, v52
	v_exp_f32_e32 v39, v39
	v_add_f32_e32 v52, v35, v52
	v_exp_f32_e32 v40, v40
	v_add_f32_e32 v52, v36, v52
	v_exp_f32_e32 v41, v41
	v_add_f32_e32 v52, v37, v52
	v_exp_f32_e32 v42, v42
	v_add_f32_e32 v52, v38, v52
	v_exp_f32_e32 v43, v43
	v_add_f32_e32 v52, v39, v52
	v_exp_f32_e32 v44, v44
	v_add_f32_e32 v52, v40, v52
	v_exp_f32_e32 v45, v45
	v_add_f32_e32 v52, v41, v52
	v_exp_f32_e32 v46, v46
	v_add_f32_e32 v52, v42, v52
	v_exp_f32_e32 v47, v47
	v_add_f32_e32 v52, v43, v52
	v_exp_f32_e32 v48, v48
	v_add_f32_e32 v52, v44, v52
	v_exp_f32_e32 v49, v49
	v_sub_f32_e32 v24, v24, v126
	v_add_f32_e32 v52, v45, v52
	v_exp_f32_e32 v24, v24
	v_sub_f32_e32 v25, v25, v126
	v_add_f32_e32 v52, v46, v52
	v_exp_f32_e32 v25, v25
	v_sub_f32_e32 v26, v26, v126
	v_add_f32_e32 v52, v47, v52
	v_exp_f32_e32 v26, v26
	v_sub_f32_e32 v27, v27, v126
	v_add_f32_e32 v52, v48, v52
	v_exp_f32_e32 v27, v27
	v_sub_f32_e32 v28, v28, v126
	v_add_f32_e32 v52, v49, v52
	v_exp_f32_e32 v28, v28
	v_sub_f32_e32 v29, v29, v126
	v_add_f32_e32 v52, v24, v52
	v_exp_f32_e32 v29, v29
	v_sub_f32_e32 v30, v30, v126
	v_add_f32_e32 v52, v25, v52
	v_exp_f32_e32 v30, v30
	v_sub_f32_e32 v31, v31, v126
	v_add_f32_e32 v52, v26, v52
	v_exp_f32_e32 v31, v31
	v_sub_f32_e32 v32, v32, v126
	v_add_f32_e32 v52, v27, v52
	v_exp_f32_e32 v32, v32
	v_sub_f32_e32 v33, v33, v126
	v_add_f32_e32 v52, v28, v52
	v_exp_f32_e32 v33, v33
	v_add_f32_e32 v52, v29, v52
	v_add_f32_e32 v52, v30, v52
	v_add_f32_e32 v52, v31, v52
	v_add_f32_e32 v52, v32, v52
	v_add_f32_e32 v52, v33, v52
	v_add_f32_e32 v52, v82, v52
	v_add_f32_e32 v52, v83, v52
	v_add_f32_e32 v52, v84, v52
	v_add_f32_e32 v52, v85, v52
	v_add_f32_e32 v52, v86, v52
	v_add_f32_e32 v52, v87, v52
	v_add_f32_e32 v52, v88, v52
	v_add_f32_e32 v52, v89, v52
	v_add_f32_e32 v52, v90, v52
	v_add_f32_e32 v52, v91, v52
	v_add_f32_e32 v52, v92, v52
	v_add_f32_e32 v52, v93, v52
	v_add_f32_e32 v52, v94, v52
	v_add_f32_e32 v52, v95, v52
	v_add_f32_e32 v52, v96, v52
	v_add_f32_e32 v52, v97, v52
	ds_bpermute_b32 v53, v172, v52
	s_waitcnt lgkmcnt(0)
	v_add_f32_e32 v52, v52, v53
	v_div_scale_f32 v53, s[6:7], v52, v52, 1.0
	v_rcp_f32_e32 v54, v53
	v_cmp_lt_f32_e64 s[0:1], 0, v52
	v_fma_f32 v55, -v53, v54, 1.0
	v_fmac_f32_e32 v54, v55, v54
	v_div_scale_f32 v55, vcc, 1.0, v52, 1.0
	v_mul_f32_e32 v56, v55, v54
	v_fma_f32 v57, -v53, v56, v55
	v_fmac_f32_e32 v56, v57, v54
	v_fma_f32 v53, -v53, v56, v55
	v_div_fmas_f32 v53, v53, v54, v56
	v_div_fixup_f32 v52, v53, v52, 1.0
	v_cndmask_b32_e64 v114, 0, v52, s[0:1]
	v_pk_mul_f32 v[2:3], v[2:3], v[114:115] op_sel_hi:[1,0]
	v_pk_mul_f32 v[6:7], v[6:7], v[114:115] op_sel_hi:[1,0]
	v_pk_mul_f32 v[116:117], v[10:11], v[114:115] op_sel_hi:[1,0]
	s_lshl_b32 s0, s4, 11
	v_lshlrev_b32_e32 v10, 5, v68
	v_pk_mul_f32 v[4:5], v[4:5], v[114:115] op_sel_hi:[1,0]
	v_pk_mul_f32 v[8:9], v[8:9], v[114:115] op_sel_hi:[1,0]
	v_pk_mul_f32 v[126:127], v[12:13], v[114:115] op_sel_hi:[1,0]
	v_or3_b32 v10, v10, s0, v74
	v_add_f32_e32 v11, v2, v3
	v_add_f32_e32 v13, v6, v7
	v_add_f32_e32 v11, v4, v11
	v_lshl_add_u32 v10, v10, 2, 0
	v_add_f32_e32 v13, v8, v13
	v_pk_mul_f32 v[128:129], v[14:15], v[114:115] op_sel_hi:[1,0]
	v_fma_f32 v11, 2.0, v11, v5
	v_add_u32_e32 v12, 0x15400, v10
	v_fma_f32 v13, 2.0, v13, v9
	v_add_u32_e32 v10, 0xd400, v10
	v_pk_mul_f32 v[130:131], v[16:17], v[114:115] op_sel_hi:[1,0]
	ds_write2_b32 v10, v11, v13 offset1:2
	ds_write2_b32 v12, v5, v9 offset1:2
	v_add_f32_e32 v11, v116, v117
	v_add_f32_e32 v13, v128, v129
	v_add_f32_e32 v11, v126, v11
	v_add_f32_e32 v13, v130, v13
	v_pk_mul_f32 v[132:133], v[18:19], v[114:115] op_sel_hi:[1,0]
	v_pk_mul_f32 v[136:137], v[22:23], v[114:115] op_sel_hi:[1,0]
	v_fma_f32 v11, 2.0, v11, v127
	v_fma_f32 v13, 2.0, v13, v131
	v_pk_mul_f32 v[134:135], v[20:21], v[114:115] op_sel_hi:[1,0]
	v_pk_mul_f32 v[138:139], v[34:35], v[114:115] op_sel_hi:[1,0]
	ds_write2_b32 v10, v11, v13 offset0:4 offset1:6
	ds_write2_b32 v12, v127, v131 offset0:4 offset1:6
	v_add_f32_e32 v11, v132, v133
	v_add_f32_e32 v13, v136, v137
	v_add_f32_e32 v11, v134, v11
	v_add_f32_e32 v13, v138, v13
	v_pk_mul_f32 v[140:141], v[36:37], v[114:115] op_sel_hi:[1,0]
	v_pk_mul_f32 v[144:145], v[40:41], v[114:115] op_sel_hi:[1,0]
	v_fma_f32 v11, 2.0, v11, v135
	v_fma_f32 v13, 2.0, v13, v139
	v_pk_mul_f32 v[142:143], v[38:39], v[114:115] op_sel_hi:[1,0]
	v_pk_mul_f32 v[146:147], v[42:43], v[114:115] op_sel_hi:[1,0]
	ds_write2_b32 v10, v11, v13 offset0:8 offset1:10
	ds_write2_b32 v12, v135, v139 offset0:8 offset1:10
	v_add_f32_e32 v11, v140, v141
	v_add_f32_e32 v13, v144, v145
	v_add_f32_e32 v11, v142, v11
	v_add_f32_e32 v13, v146, v13
	v_pk_mul_f32 v[60:61], v[44:45], v[114:115] op_sel_hi:[1,0]
	v_pk_mul_f32 v[64:65], v[48:49], v[114:115] op_sel_hi:[1,0]
	v_fma_f32 v11, 2.0, v11, v143
	v_fma_f32 v13, 2.0, v13, v147
	v_pk_mul_f32 v[62:63], v[46:47], v[114:115] op_sel_hi:[1,0]
	v_pk_mul_f32 v[66:67], v[24:25], v[114:115] op_sel_hi:[1,0]
; #define LAS __attribute__((address_space(3)))
; __device__ __forceinline__ unsigned cvt_pk_bf16(float lo, float hi) { f32x2_t v = {lo, hi}; bf16x2_t b = __builtin_convertvector(v, bf16x2_t); return __builtin_bit_cast(unsigned, b); }
; #define MFMA32(a, b, c) __builtin_amdgcn_mfma_f32_32x32x16_bf16((a), (b), (c), 0, 0, 0)
; __device__ __forceinline__ void unit(LAS unsigned char* lds, const bf16* Z, const bf16* kct, const bf16* vct, bf16* OAp, int b, int g, int iq, const int tid_in) {
;     ...
;                 IA[(j * 64 + tl) * 32 + n] = 2.f * (p[blk][4 * rq] + p[blk][4 * rq + 1] + p[blk][4 * rq + 2]) + p[blk][4 * rq + 3];
;                 IB[(j * 64 + tl) * 32 + n] = p[blk][4 * rq + 3]; }
;         f32x16 oc[2];
; #pragma unroll
;         for (int r = 0; r < 16; ++r) { oc[0][r] = 0.f; oc[1][r] = 0.f; }
; #pragma unroll
;         for (int s = 0; s < 8; ++s) { const int blk = s >> 1, rb = 8 * (s & 1);
;             u32x4 pw; pw.x = cvt_pk_bf16(p[blk][rb + 0], p[blk][rb + 1]); pw.y = cvt_pk_bf16(p[blk][rb + 2], p[blk][rb + 3]); pw.z = cvt_pk_bf16(p[blk][rb + 4], p[blk][rb + 5]); pw.w = cvt_pk_bf16(p[blk][rb + 6], p[blk][rb + 7]);
;             const bf16x8 pa = __builtin_bit_cast(bf16x8, pw);
; #pragma unroll
;             for (int db = 0; db < 2; ++db) { const bf16x8 vf = *(const LAS bf16x8*)(VC + (32 * db + r32) * VST2 + 16 * s + 8 * hi); oc[db] = MFMA32(vf, pa, oc[db]); } }
; #pragma unroll
;         for (int r = 0; r < 16; ++r) { otot[0][r] += gate[0] * oc[0][r]; otot[1][r] += gate[0] * oc[1][r]; }
;     }
;     __syncthreads();
;     {
;         const int n = lane & 31;
; #pragma unroll
;         for (int q = 0; q < 4; ++q) { const int tk = (tid >> 5) + 16 * q;
;             float imp = 0.f;
; #pragma unroll
;             for (int jj = 0; jj < 4; ++jj) { imp += IA[(jj * 64 + tk) * 32 + n]; if (n > 0) imp += IB[(jj * 64 + tk) * 32 + n - 1]; }
	ds_write2_b32 v10, v11, v13 offset0:12 offset1:14
	ds_write2_b32 v12, v143, v147 offset0:12 offset1:14
	v_add_f32_e32 v11, v60, v61
	v_add_f32_e32 v13, v64, v65
	v_add_f32_e32 v11, v62, v11
	v_add_f32_e32 v13, v66, v13
	v_pk_mul_f32 v[52:53], v[26:27], v[114:115] op_sel_hi:[1,0]
	v_pk_mul_f32 v[56:57], v[30:31], v[114:115] op_sel_hi:[1,0]
	v_fma_f32 v11, 2.0, v11, v63
	v_fma_f32 v13, 2.0, v13, v67
	v_pk_mul_f32 v[54:55], v[28:29], v[114:115] op_sel_hi:[1,0]
	v_pk_mul_f32 v[58:59], v[32:33], v[114:115] op_sel_hi:[1,0]
	ds_write2_b32 v10, v11, v13 offset0:16 offset1:18
	ds_write2_b32 v12, v63, v67 offset0:16 offset1:18
	v_add_f32_e32 v11, v52, v53
	v_add_f32_e32 v13, v56, v57
	v_add_f32_e32 v11, v54, v11
	v_add_f32_e32 v13, v58, v13
	v_pk_mul_f32 v[42:43], v[82:83], v[114:115] op_sel_hi:[1,0]
	v_pk_mul_f32 v[46:47], v[86:87], v[114:115] op_sel_hi:[1,0]
	v_fma_f32 v11, 2.0, v11, v55
	v_fma_f32 v13, 2.0, v13, v59
	v_pk_mul_f32 v[44:45], v[84:85], v[114:115] op_sel_hi:[1,0]
	v_pk_mul_f32 v[48:49], v[88:89], v[114:115] op_sel_hi:[1,0]
	ds_write2_b32 v10, v11, v13 offset0:20 offset1:22
	ds_write2_b32 v12, v55, v59 offset0:20 offset1:22
	v_add_f32_e32 v11, v42, v43
	v_add_f32_e32 v13, v46, v47
	v_add_f32_e32 v11, v44, v11
	v_add_f32_e32 v13, v48, v13
	v_pk_mul_f32 v[34:35], v[90:91], v[114:115] op_sel_hi:[1,0]
	v_pk_mul_f32 v[38:39], v[94:95], v[114:115] op_sel_hi:[1,0]
	v_fma_f32 v11, 2.0, v11, v45
	v_fma_f32 v13, 2.0, v13, v49
	v_pk_mul_f32 v[36:37], v[92:93], v[114:115] op_sel_hi:[1,0]
	v_pk_mul_f32 v[40:41], v[96:97], v[114:115] op_sel_hi:[1,0]
	ds_write2_b32 v10, v11, v13 offset0:24 offset1:26
	ds_write2_b32 v12, v45, v49 offset0:24 offset1:26
	v_add_f32_e32 v11, v34, v35
	v_add_f32_e32 v13, v38, v39
	v_add_f32_e32 v11, v36, v11
	v_add_f32_e32 v13, v40, v13
	v_fma_f32 v11, 2.0, v11, v37
	v_fma_f32 v13, 2.0, v13, v41
	s_movk_i32 s0, 0x110
	ds_write2_b32 v10, v11, v13 offset0:28 offset1:30
	ds_write2_b32 v12, v37, v41 offset0:28 offset1:30
	v_mad_u32_u24 v81, v73, s0, v76
	v_cvt_pk_bf16_f32 v2, v2, v3
	v_cvt_pk_bf16_f32 v3, v4, v5
	v_cvt_pk_bf16_f32 v4, v6, v7
	v_cvt_pk_bf16_f32 v5, v8, v9
	ds_read_b128 v[6:9], v81 offset:36864
	ds_read_b128 v[82:85], v81 offset:36896
	s_waitcnt lgkmcnt(1)
	v_mfma_f32_32x32x16_bf16 v[18:33], v[6:9], v[2:5], 0
	ds_read_b128 v[6:9], v81 offset:45568
	v_cvt_pk_bf16_f32 v86, v116, v117
	v_cvt_pk_bf16_f32 v87, v126, v127
	v_cvt_pk_bf16_f32 v88, v128, v129
	v_cvt_pk_bf16_f32 v89, v130, v131
	v_cvt_pk_bf16_f32 v60, v60, v61
	v_cvt_pk_bf16_f32 v61, v62, v63
	s_waitcnt lgkmcnt(1)
	v_mfma_f32_32x32x16_bf16 v[18:33], v[82:85], v[86:89], v[18:33]
	ds_read_b128 v[82:85], v81 offset:45600
	v_cvt_pk_bf16_f32 v62, v64, v65
	v_cvt_pk_bf16_f32 v63, v66, v67
	ds_read_b128 v[64:67], v81 offset:36992
	v_cvt_pk_bf16_f32 v52, v52, v53
	v_cvt_pk_bf16_f32 v53, v54, v55
	v_cvt_pk_bf16_f32 v54, v56, v57
	s_waitcnt lgkmcnt(2)
	v_mfma_f32_32x32x16_bf16 v[2:17], v[6:9], v[2:5], 0
	v_cvt_pk_bf16_f32 v55, v58, v59
	ds_read_b128 v[56:59], v81 offset:37024
	v_cvt_pk_bf16_f32 v42, v42, v43
	v_cvt_pk_bf16_f32 v43, v44, v45
	v_cvt_pk_bf16_f32 v44, v46, v47
	v_cvt_pk_bf16_f32 v45, v48, v49
	ds_read_b128 v[46:49], v81 offset:37056
	s_waitcnt lgkmcnt(3)
	v_mfma_f32_32x32x16_bf16 v[2:17], v[82:85], v[86:89], v[2:17]
	ds_read_b128 v[86:89], v81 offset:36928
	v_cvt_pk_bf16_f32 v82, v132, v133
	v_cvt_pk_bf16_f32 v83, v134, v135
	v_cvt_pk_bf16_f32 v84, v136, v137
	v_cvt_pk_bf16_f32 v85, v138, v139
	v_cvt_pk_bf16_f32 v34, v34, v35
	v_cvt_pk_bf16_f32 v35, v36, v37
	s_waitcnt lgkmcnt(0)
	v_mfma_f32_32x32x16_bf16 v[18:33], v[86:89], v[82:85], v[18:33]
	ds_read_b128 v[86:89], v81 offset:45632
	v_cvt_pk_bf16_f32 v36, v38, v39
	v_cvt_pk_bf16_f32 v37, v40, v41
	ds_read_b128 v[38:41], v81 offset:37088
	v_cmp_ne_u32_e64 s[0:1], 0, v73
	s_waitcnt lgkmcnt(1)
	v_mfma_f32_32x32x16_bf16 v[2:17], v[86:89], v[82:85], v[2:17]
	ds_read_b128 v[86:89], v81 offset:36960
	v_cvt_pk_bf16_f32 v82, v140, v141
	v_cvt_pk_bf16_f32 v83, v142, v143
	v_cvt_pk_bf16_f32 v84, v144, v145
	v_cvt_pk_bf16_f32 v85, v146, v147
	s_waitcnt lgkmcnt(0)
	s_nop 0
	v_mfma_f32_32x32x16_bf16 v[18:33], v[86:89], v[82:85], v[18:33]
	ds_read_b128 v[86:89], v81 offset:45664
	v_mfma_f32_32x32x16_bf16 v[18:33], v[64:67], v[60:63], v[18:33]
	ds_read_b128 v[64:67], v81 offset:45696
	s_waitcnt lgkmcnt(1)
	v_mfma_f32_32x32x16_bf16 v[2:17], v[86:89], v[82:85], v[2:17]
	v_mfma_f32_32x32x16_bf16 v[18:33], v[56:59], v[52:55], v[18:33]
	ds_read_b128 v[56:59], v81 offset:45728
	s_waitcnt lgkmcnt(1)
	v_mfma_f32_32x32x16_bf16 v[2:17], v[64:67], v[60:63], v[2:17]
	v_mfma_f32_32x32x16_bf16 v[18:33], v[46:49], v[42:45], v[18:33]
	ds_read_b128 v[46:49], v81 offset:45760
	s_waitcnt lgkmcnt(1)
	v_mfma_f32_32x32x16_bf16 v[2:17], v[56:59], v[52:55], v[2:17]
	v_mfma_f32_32x32x16_bf16 v[18:33], v[38:41], v[34:37], v[18:33]
	ds_read_b128 v[38:41], v81 offset:45792
	s_waitcnt lgkmcnt(0)
	s_barrier
	v_mfma_f32_32x32x16_bf16 v[2:17], v[46:49], v[42:45], v[2:17]
	v_mfma_f32_32x32x16_bf16 v[2:17], v[38:41], v[34:37], v[2:17]
	v_lshl_add_u32 v34, v78, 2, 0
	ds_read_b32 v35, v34 offset:54272
	v_lshlrev_b32_e32 v36, 2, v78
	s_waitcnt lgkmcnt(0)
	v_add_f32_e32 v35, 0, v35
	s_and_saveexec_b64 s[4:5], s[0:1]
	s_cbranch_execz .LBB0_418
	s_add_i32 s6, 0, 0x15400
	v_add3_u32 v37, s6, v36, -4
	ds_read_b32 v37, v37
	s_waitcnt lgkmcnt(0)
	v_add_f32_e32 v35, v35, v37
